# P4: head-norm gain vector loaded once before the row loop (was reloaded and waited for before every store, behind the previous store's ack)
# baseline (speedup 1.0000x reference)
; DI int opaque_tid() { int t = threadIdx.x; asm volatile("" : "+v"(t)); return t; }
; DI void p4_store(const P4Row& R, const float* hg, bf16_t* YC, int row, int lane) {
;     ...
;         ss += __shfl_xor(ss, 1); ss += __shfl_xor(ss, 2); ss += __shfl_xor(ss, 4); ss += __shfl_xor(ss, 8);
;         const float rinv = rsqrtf(ss * (1.0f / 128.0f) + EPS);
;         const f32x4 g0 = *(const f32x4*)(hg + c0), g1 = *(const f32x4*)(hg + c0 + 4);
; DI void p4_fixups(Frame& F, ArgsP A) {
;     const int ftid = opaque_tid(), flane = ftid & 63;
;     const bf16_t* OH = (const bf16_t*)(A->ws + WS_OH); const bf16_t* SG = (const bf16_t*)(A->ws + WS_SG); const float* hg = A->in[4];
;     const bf16_t* OG = (const bf16_t*)(A->ws + WS_OG); const float* LSE = (const float*)(A->ws + WS_LSE);
;     bf16_t* YC = (bf16_t*)(A->ws + WS_YCAT);
;     const int gw = F.vcu * NWAVES + F.wave, NGW = F.G * NWAVES, lane = flane;
;     for (int row = gw; row < T; row += 2 * NGW) {
.LBB0_524:
	s_cmp_lt_i32 s60, 5
	s_cselect_b64 s[4:5], -1, 0
	s_cmp_gt_i32 s61, 4
	s_cselect_b64 s[6:7], -1, 0
	s_and_b64 s[4:5], s[4:5], s[6:7]
	s_andn2_b64 vcc, exec, s[4:5]
	s_cbranch_vccnz .LBB0_578
	s_lshl_b32 s3, s58, 3
	s_add_i32 s6, s3, s59
	s_mov_b64 s[4:5], s[0:1]
	v_mov_b32_e32 v1, v0
	s_cmpk_gt_i32 s6, 0x3fff
	s_cbranch_scc1 .LBB0_532
	s_load_dwordx2 s[8:9], s[4:5], 0x98
	s_load_dwordx2 s[10:11], s[4:5], 0x20
	s_waitcnt vmcnt(0)
	v_and_b32_e32 v3, 63, v1
	v_lshrrev_b32_e32 v1, 2, v1
	v_mov_b32_e32 v5, 0
	v_and_b32_e32 v4, 12, v1
	s_waitcnt lgkmcnt(0)
	v_lshl_add_u64 v[10:11], s[8:9], 0, v[4:5]
	s_mov_b64 s[4:5], 0x300000
	v_mbcnt_lo_u32_b32 v1, -1, 0
	v_lshlrev_b32_e32 v2, 3, v3
	v_lshlrev_b32_e32 v6, 5, v3
	v_lshl_add_u64 v[90:91], v[10:11], 0, s[4:5]
	v_lshlrev_b32_e32 v10, 4, v3
	v_mbcnt_hi_u32_b32 v3, -1, v1
	v_and_b32_e32 v7, 64, v3
	v_xor_b32_e32 v1, 1, v3
	v_add_u32_e32 v7, 64, v7
	v_cmp_lt_i32_e32 vcc, v1, v7
	v_xor_b32_e32 v9, 2, v3
	v_mov_b32_e32 v11, v5
	v_cndmask_b32_e32 v1, v3, v1, vcc
	v_cmp_lt_i32_e32 vcc, v9, v7
	v_lshl_add_u64 v[12:13], s[8:9], 0, v[10:11]
	s_mov_b64 s[4:5], 0x2f200000
	v_cndmask_b32_e32 v9, v3, v9, vcc
	v_lshlrev_b32_e32 v118, 2, v9
	v_xor_b32_e32 v9, 4, v3
	v_cmp_lt_i32_e32 vcc, v9, v7
	v_lshl_add_u64 v[92:93], v[12:13], 0, s[4:5]
	s_mov_b64 s[4:5], 0x2b200000
	v_cndmask_b32_e32 v9, v3, v9, vcc
	v_lshlrev_b32_e32 v119, 2, v9
	v_xor_b32_e32 v9, 8, v3
	s_add_u32 s3, s8, 0x32300000
	v_cmp_lt_i32_e32 vcc, v9, v7
	v_mov_b32_e32 v7, v5
	v_lshl_add_u64 v[100:101], v[12:13], 0, s[4:5]
	s_mov_b64 s[4:5], 0x16200000
	s_addc_u32 s21, s9, 0
	v_or_b32_e32 v8, 0x600, v2
	v_lshl_add_u64 v[94:95], s[10:11], 0, v[6:7]
	v_or_b32_e32 v6, 0x1000, v6
	v_lshl_add_u64 v[102:103], v[12:13], 0, s[4:5]
	s_ashr_i32 s7, s6, 31
	s_mul_hi_i32 s4, s6, 0x1400
	s_mul_i32 s5, s6, 0x1400
	v_lshl_add_u64 v[96:97], s[10:11], 0, v[6:7]
	v_lshlrev_b32_e32 v6, 2, v8
	v_or_b32_e32 v104, s5, v10
	v_mov_b32_e32 v105, s4
	s_lshl_b64 s[4:5], s[6:7], 10
	v_lshl_add_u64 v[98:99], s[10:11], 0, v[6:7]
	s_lshl_b32 s10, s33, 4
	v_or_b32_e32 v106, s4, v10
	v_mov_b32_e32 v107, s5
	s_lshl_b64 s[4:5], s[6:7], 4
	v_cndmask_b32_e32 v3, v3, v9, vcc
	s_ashr_i32 s11, s10, 31
	v_or_b32_e32 v108, s4, v4
	v_mov_b32_e32 v109, s5
	s_lshl_b64 s[4:5], s[6:7], 12
	s_lshl_b32 s23, s33, 3
	v_lshlrev_b32_e32 v1, 2, v1
	v_lshlrev_b32_e32 v120, 2, v3
	s_mul_i32 s12, s33, 0x14000
	s_mul_hi_i32 s13, s10, 0x1400
	s_lshl_b64 s[14:15], s[10:11], 10
	s_lshl_b64 s[16:17], s[10:11], 4
	v_or_b32_e32 v110, s4, v10
	v_mov_b32_e32 v111, s5
	s_lshl_b64 s[18:19], s[10:11], 12
	s_mov_b32 s7, 0x2b200000
	s_mov_b32 s11, 0x16200000
	s_mov_b32 s26, 0x300000
	s_mov_b32 s27, 0x340000
	s_mov_b32 s28, 0x380000
	s_brev_b32 s20, 60
	s_mov_b32 s22, 0x358637bd
	s_mov_b32 s29, 0x800000
	s_mov_b32 s30, 0x32300000
	s_mov_b32 s31, 0x32301000
	v_lshlrev_b32_e32 v121, 1, v2
	v_lshlrev_b32_e32 v122, 1, v8
	global_load_dwordx4 v[160:163], v[94:95], off offset:16
	global_load_dwordx4 v[164:167], v[94:95], off
	global_load_dwordx4 v[168:171], v[94:95], off offset:2048
	global_load_dwordx4 v[172:175], v[94:95], off offset:2064
	global_load_dwordx4 v[176:179], v[96:97], off offset:16
	global_load_dwordx4 v[180:183], v[96:97], off
	global_load_dwordx4 v[184:187], v[98:99], off offset:16
	global_load_dwordx4 v[188:191], v[98:99], off
	s_waitcnt vmcnt(0)
	s_branch .LBB0_528

; DI unsigned pk2(float lo, float hi) { return cvtpk_s(lo, hi); }
; DI void p4_store(const P4Row& R, const float* hg, bf16_t* YC, int row, int lane) {
; #pragma unroll
;     for (int j = 0; j < 4; ++j) {
;         const int c0 = 512 * j + 8 * lane; const u32x4 o = R.o[j], sg = R.sg[j];
;         float v[8] = {bflo(o.x), bfhi(o.x), bflo(o.y), bfhi(o.y), bflo(o.z), bfhi(o.z), bflo(o.w), bfhi(o.w)};
;         const float s[8] = {bflo(sg.x), bfhi(sg.x), bflo(sg.y), bfhi(sg.y), bflo(sg.z), bfhi(sg.z), bflo(sg.w), bfhi(sg.w)};
;         float ss = 0.f;
; #pragma unroll
;         for (int e = 0; e < 8; ++e) ss += v[e] * v[e];
;         ss += __shfl_xor(ss, 1); ss += __shfl_xor(ss, 2); ss += __shfl_xor(ss, 4); ss += __shfl_xor(ss, 8);
;         const float rinv = rsqrtf(ss * (1.0f / 128.0f) + EPS);
;         const f32x4 g0 = *(const f32x4*)(hg + c0), g1 = *(const f32x4*)(hg + c0 + 4);
; #pragma unroll
;         for (int e = 0; e < 4; ++e) { v[e] = v[e] * rinv * g0[e] * s[e]; v[4 + e] = v[4 + e] * rinv * g1[e] * s[4 + e]; }
;         u32x4 w; w.x = pk2(v[0], v[1]); w.y = pk2(v[2], v[3]); w.z = pk2(v[4], v[5]); w.w = pk2(v[6], v[7]);
;         *(u32x4*)(YC + (size_t)row * KCAT + 512 + c0) = w;
;     }
.LBB0_530:
	s_nop 0
	s_waitcnt vmcnt(0)
	v_and_b32_e32 v143, 0xffff0000, v86
	v_and_b32_e32 v153, 0xffff0000, v82
	v_lshlrev_b32_e32 v138, 16, v87
	v_and_b32_e32 v139, 0xffff0000, v87
	v_lshlrev_b32_e32 v142, 16, v86
	v_lshlrev_b32_e32 v148, 16, v83
	v_and_b32_e32 v149, 0xffff0000, v83
	v_lshlrev_b32_e32 v152, 16, v82
	v_mov_b32_e32 v154, v153
	v_mov_b32_e32 v155, v143
	v_pk_mul_f32 v[140:141], v[138:139], v[138:139]
	v_pk_mul_f32 v[150:151], v[148:149], v[148:149]
	v_mov_b32_e32 v82, v152
	v_mov_b32_e32 v83, v142
	v_pk_mul_f32 v[154:155], v[154:155], v[154:155]
	v_lshlrev_b32_e32 v136, 16, v88
	v_and_b32_e32 v137, 0xffff0000, v88
	v_lshlrev_b32_e32 v146, 16, v84
	v_and_b32_e32 v147, 0xffff0000, v84
	v_pk_fma_f32 v[82:83], v[82:83], v[82:83], v[154:155]
	v_mov_b32_e32 v154, v150
	v_mov_b32_e32 v155, v140
	v_lshlrev_b32_e32 v116, 16, v89
	v_and_b32_e32 v117, 0xffff0000, v89
	v_pk_mul_f32 v[88:89], v[136:137], v[136:137]
	v_lshlrev_b32_e32 v144, 16, v85
	v_and_b32_e32 v145, 0xffff0000, v85
	v_pk_mul_f32 v[84:85], v[146:147], v[146:147]
	v_pk_add_f32 v[82:83], v[154:155], v[82:83]
	v_mov_b32_e32 v140, v151
	v_pk_add_f32 v[82:83], v[140:141], v[82:83]
	v_mov_b32_e32 v140, v84
	v_mov_b32_e32 v141, v88
	v_pk_mul_f32 v[134:135], v[116:117], v[116:117]
	v_pk_mul_f32 v[86:87], v[144:145], v[144:145]
	v_pk_add_f32 v[82:83], v[140:141], v[82:83]
	v_mov_b32_e32 v88, v85
	v_pk_add_f32 v[82:83], v[88:89], v[82:83]
	v_mov_b32_e32 v84, v86
	v_mov_b32_e32 v85, v134
	v_pk_add_f32 v[82:83], v[84:85], v[82:83]
	v_mov_b32_e32 v134, v87
	v_pk_add_f32 v[82:83], v[134:135], v[82:83]
	ds_bpermute_b32 v85, v1, v83
	ds_bpermute_b32 v84, v1, v82
	v_lshlrev_b32_e32 v86, 16, v81
	v_and_b32_e32 v87, 0xffff0000, v81
	v_lshlrev_b32_e32 v88, 16, v80
	v_and_b32_e32 v89, 0xffff0000, v80
	s_waitcnt lgkmcnt(0)
	v_pk_add_f32 v[82:83], v[82:83], v[84:85]
	ds_bpermute_b32 v85, v118, v83
	ds_bpermute_b32 v84, v118, v82
	v_lshlrev_b32_e32 v140, 16, v79
	v_and_b32_e32 v141, 0xffff0000, v79
	v_max3_f32 v129, v126, v127, v128
	s_waitcnt lgkmcnt(0)
	v_pk_add_f32 v[82:83], v[82:83], v[84:85]
	ds_bpermute_b32 v85, v119, v83
	ds_bpermute_b32 v84, v119, v82
	s_waitcnt lgkmcnt(0)
	v_pk_add_f32 v[84:85], v[82:83], v[84:85]
	ds_bpermute_b32 v135, v120, v85
	ds_bpermute_b32 v134, v120, v84
	v_mov_b64_e32 v[82:83], s[22:23]
	s_waitcnt lgkmcnt(0)
	v_pk_add_f32 v[80:81], v[84:85], v[134:135]
	s_nop 0
	v_pk_fma_f32 v[150:151], v[80:81], s[20:21], v[82:83] op_sel_hi:[1,0,0]
	v_lshlrev_b32_e32 v84, 16, v78
	v_mul_f32_e32 v79, 0x4b800000, v151
	v_cmp_gt_f32_e32 vcc, s29, v151
	v_and_b32_e32 v85, 0xffff0000, v78
	v_lshl_add_u64 v[80:81], s[8:9], 0, v[104:105]
	v_cndmask_b32_e32 v79, v151, v79, vcc
	v_rsq_f32_e32 v79, v79
	s_nop 0
	v_mul_f32_e32 v78, 0x45800000, v79
	v_cndmask_b32_e32 v78, v79, v78, vcc
	v_pk_mul_f32 v[134:135], v[78:79], v[142:143] op_sel_hi:[0,1]
	v_pk_mul_f32 v[136:137], v[78:79], v[136:137] op_sel_hi:[0,1]
	v_pk_mul_f32 v[138:139], v[78:79], v[138:139] op_sel_hi:[0,1]
	v_pk_mul_f32 v[78:79], v[78:79], v[116:117] op_sel_hi:[0,1]
	v_pk_mul_f32 v[78:79], v[162:163], v[78:79]
	v_pk_mul_f32 v[130:131], v[164:165], v[134:135]
	v_pk_mul_f32 v[112:113], v[160:161], v[136:137]
	v_pk_mul_f32 v[132:133], v[166:167], v[138:139]
	v_pk_mul_f32 v[78:79], v[78:79], v[86:87]
	v_pk_mul_f32 v[84:85], v[130:131], v[84:85]
	v_pk_mul_f32 v[88:89], v[112:113], v[88:89]
	v_pk_mul_f32 v[112:113], v[132:133], v[140:141]
	v_cvt_pk_bf16_f32 v87, v78, v79
	v_add_co_u32_e32 v78, vcc, s30, v80
	v_cvt_pk_bf16_f32 v84, v84, v85
	v_cvt_pk_bf16_f32 v85, v112, v113
	v_cvt_pk_bf16_f32 v86, v88, v89
	v_addc_co_u32_e32 v79, vcc, 0, v81, vcc
	global_store_dwordx4 v[78:79], v[84:87], off offset:1024
	s_nop 1
	v_lshlrev_b32_e32 v86, 16, v65
	v_and_b32_e32 v87, 0xffff0000, v65
	v_mul_f32_e32 v65, 0x4b800000, v150
	v_cmp_gt_f32_e32 vcc, s29, v150
	v_lshlrev_b32_e32 v116, 16, v71
	v_and_b32_e32 v117, 0xffff0000, v71
	v_cndmask_b32_e32 v65, v150, v65, vcc
	v_rsq_f32_e32 v65, v65
	v_lshlrev_b32_e32 v114, 16, v72
	v_and_b32_e32 v115, 0xffff0000, v72
	v_lshlrev_b32_e32 v84, 16, v77
	v_mul_f32_e32 v71, 0x45800000, v65
	v_cndmask_b32_e32 v72, v65, v71, vcc
	v_and_b32_e32 v85, 0xffff0000, v77
	v_lshlrev_b32_e32 v138, 16, v76
	v_and_b32_e32 v139, 0xffff0000, v76
	v_lshlrev_b32_e32 v76, 16, v75
	v_and_b32_e32 v77, 0xffff0000, v75
	v_lshlrev_b32_e32 v140, 16, v74
	v_and_b32_e32 v141, 0xffff0000, v74
	v_lshlrev_b32_e32 v88, 16, v73
	v_and_b32_e32 v89, 0xffff0000, v73
	v_pk_mul_f32 v[74:75], v[72:73], v[152:153] op_sel_hi:[0,1]
	v_pk_mul_f32 v[142:143], v[72:73], v[146:147] op_sel_hi:[0,1]
	v_pk_mul_f32 v[146:147], v[72:73], v[148:149] op_sel_hi:[0,1]
	v_pk_mul_f32 v[72:73], v[72:73], v[144:145] op_sel_hi:[0,1]
	v_and_b32_e32 v71, 0xffff0000, v69
	v_lshlrev_b32_e32 v112, 16, v64
	v_and_b32_e32 v113, 0xffff0000, v64
	v_lshlrev_b32_e32 v64, 16, v60
	v_and_b32_e32 v65, 0xffff0000, v60
	v_lshlrev_b32_e32 v60, 16, v59
	v_pk_mul_f32 v[74:75], v[168:169], v[74:75]
	v_pk_mul_f32 v[130:131], v[172:173], v[142:143]
	v_pk_mul_f32 v[132:133], v[170:171], v[146:147]
	v_pk_mul_f32 v[72:73], v[174:175], v[72:73]
	v_pk_mul_f32 v[74:75], v[74:75], v[140:141]
	v_pk_mul_f32 v[130:131], v[130:131], v[138:139]
	v_pk_mul_f32 v[76:77], v[132:133], v[76:77]
	v_pk_mul_f32 v[84:85], v[72:73], v[84:85]
	v_cvt_pk_bf16_f32 v72, v74, v75
	v_cvt_pk_bf16_f32 v73, v76, v77
	v_cvt_pk_bf16_f32 v74, v130, v131
	v_cvt_pk_bf16_f32 v75, v84, v85
	global_store_dwordx4 v[78:79], v[72:75], off offset:2048
	s_nop 0
	v_and_b32_e32 v135, 0xffff0000, v70
	v_and_b32_e32 v85, 0xffff0000, v66
	v_lshlrev_b32_e32 v134, 16, v70
	v_lshlrev_b32_e32 v70, 16, v69
	v_lshlrev_b32_e32 v76, 16, v68
; DI unsigned pk2(float lo, float hi) { return cvtpk_s(lo, hi); }
; DI void p4_store(const P4Row& R, const float* hg, bf16_t* YC, int row, int lane) {
; #pragma unroll
;     for (int j = 0; j < 4; ++j) {
;         const int c0 = 512 * j + 8 * lane; const u32x4 o = R.o[j], sg = R.sg[j];
;         float v[8] = {bflo(o.x), bfhi(o.x), bflo(o.y), bfhi(o.y), bflo(o.z), bfhi(o.z), bflo(o.w), bfhi(o.w)};
;         const float s[8] = {bflo(sg.x), bfhi(sg.x), bflo(sg.y), bfhi(sg.y), bflo(sg.z), bfhi(sg.z), bflo(sg.w), bfhi(sg.w)};
;         float ss = 0.f;
; #pragma unroll
;         for (int e = 0; e < 8; ++e) ss += v[e] * v[e];
;         ss += __shfl_xor(ss, 1); ss += __shfl_xor(ss, 2); ss += __shfl_xor(ss, 4); ss += __shfl_xor(ss, 8);
;         const float rinv = rsqrtf(ss * (1.0f / 128.0f) + EPS);
;         const f32x4 g0 = *(const f32x4*)(hg + c0), g1 = *(const f32x4*)(hg + c0 + 4);
; #pragma unroll
;         for (int e = 0; e < 4; ++e) { v[e] = v[e] * rinv * g0[e] * s[e]; v[4 + e] = v[4 + e] * rinv * g1[e] * s[4 + e]; }
;         u32x4 w; w.x = pk2(v[0], v[1]); w.y = pk2(v[2], v[3]); w.z = pk2(v[4], v[5]); w.w = pk2(v[6], v[7]);
;         *(u32x4*)(YC + (size_t)row * KCAT + 512 + c0) = w;
;     }
;     {
;         const int c0 = 8 * lane; const float l0 = R.l0, l1 = R.l1, l2 = R.l2; const u32x4 x0 = R.x0, x1 = R.x1, x2 = R.x2;
;         const float mx = fmaxf(l0, fmaxf(l1, l2)); float a0 = __expf(l0 - mx), a1 = __expf(l1 - mx), a2 = __expf(l2 - mx);
;         const float inv = 1.0f / (a0 + a1 + a2); a0 *= inv; a1 *= inv; a2 *= inv;
;         u32x4 w;
;         w.x = pk2(a0 * bflo(x0.x) + a1 * bflo(x1.x) + a2 * bflo(x2.x), a0 * bfhi(x0.x) + a1 * bfhi(x1.x) + a2 * bfhi(x2.x));
;         w.y = pk2(a0 * bflo(x0.y) + a1 * bflo(x1.y) + a2 * bflo(x2.y), a0 * bfhi(x0.y) + a1 * bfhi(x1.y) + a2 * bfhi(x2.y));
;         w.z = pk2(a0 * bflo(x0.z) + a1 * bflo(x1.z) + a2 * bflo(x2.z), a0 * bfhi(x0.z) + a1 * bfhi(x1.z) + a2 * bfhi(x2.z));
;         w.w = pk2(a0 * bflo(x0.w) + a1 * bflo(x1.w) + a2 * bflo(x2.w), a0 * bfhi(x0.w) + a1 * bfhi(x1.w) + a2 * bfhi(x2.w));
;         *(u32x4*)(YC + (size_t)row * KCAT + c0) = w;
;     }
; }
	v_and_b32_e32 v77, 0xffff0000, v68
	v_lshlrev_b32_e32 v68, 16, v67
	v_and_b32_e32 v69, 0xffff0000, v67
	v_lshlrev_b32_e32 v84, 16, v66
	v_mov_b32_e32 v148, v85
	v_mov_b32_e32 v149, v135
	v_pk_mul_f32 v[66:67], v[88:89], v[88:89]
	v_pk_mul_f32 v[136:137], v[114:115], v[114:115]
	v_pk_mul_f32 v[138:139], v[116:117], v[116:117]
	v_pk_mul_f32 v[140:141], v[70:71], v[70:71]
	v_pk_mul_f32 v[142:143], v[76:77], v[76:77]
	v_pk_mul_f32 v[144:145], v[68:69], v[68:69]
	v_mov_b32_e32 v146, v84
	v_mov_b32_e32 v147, v134
	v_pk_mul_f32 v[148:149], v[148:149], v[148:149]
	v_mov_b32_e32 v150, v144
	v_mov_b32_e32 v151, v138
	v_mov_b32_e32 v138, v145
	v_mov_b32_e32 v144, v142
	v_mov_b32_e32 v145, v136
	v_mov_b32_e32 v136, v143
	v_mov_b32_e32 v142, v140
	v_mov_b32_e32 v143, v66
	v_mov_b32_e32 v66, v141
	v_pk_fma_f32 v[140:141], v[146:147], v[146:147], v[148:149]
	s_nop 0
	v_pk_add_f32 v[140:141], v[150:151], v[140:141]
	s_nop 0
	v_pk_add_f32 v[138:139], v[138:139], v[140:141]
	v_lshlrev_b32_e32 v140, 16, v62
	v_pk_add_f32 v[138:139], v[144:145], v[138:139]
	v_and_b32_e32 v141, 0xffff0000, v62
	v_pk_add_f32 v[136:137], v[136:137], v[138:139]
	v_lshlrev_b32_e32 v138, 16, v63
	v_pk_add_f32 v[136:137], v[142:143], v[136:137]
	v_and_b32_e32 v139, 0xffff0000, v63
	v_pk_add_f32 v[66:67], v[66:67], v[136:137]
	ds_bpermute_b32 v137, v1, v67
	ds_bpermute_b32 v136, v1, v66
	v_lshlrev_b32_e32 v62, 16, v61
	v_and_b32_e32 v63, 0xffff0000, v61
	v_and_b32_e32 v61, 0xffff0000, v59
	v_and_b32_e32 v59, 0xffff0000, v46
	s_waitcnt lgkmcnt(0)
	v_pk_add_f32 v[66:67], v[66:67], v[136:137]
	ds_bpermute_b32 v137, v118, v67
	ds_bpermute_b32 v136, v118, v66
	s_waitcnt lgkmcnt(0)
	v_pk_add_f32 v[136:137], v[66:67], v[136:137]
	ds_bpermute_b32 v143, v119, v137
	ds_bpermute_b32 v142, v119, v136
	v_lshlrev_b32_e32 v66, 16, v58
	v_and_b32_e32 v67, 0xffff0000, v58
	v_lshlrev_b32_e32 v58, 16, v54
	s_waitcnt lgkmcnt(0)
	v_pk_add_f32 v[136:137], v[136:137], v[142:143]
	ds_bpermute_b32 v143, v120, v137
	ds_bpermute_b32 v142, v120, v136
	s_waitcnt lgkmcnt(0)
	v_pk_add_f32 v[136:137], v[136:137], v[142:143]
	s_nop 0
	v_pk_fma_f32 v[82:83], v[136:137], s[20:21], v[82:83] op_sel_hi:[1,0,0]
	v_and_b32_e32 v137, 0xffff0000, v54
	v_mul_f32_e32 v136, 0x4b800000, v83
	v_cmp_gt_f32_e32 vcc, s29, v83
	v_lshlrev_b32_e32 v54, 16, v56
	v_lshlrev_b32_e32 v142, 16, v50
	v_cndmask_b32_e32 v83, v83, v136, vcc
	v_rsq_f32_e32 v83, v83
	v_lshlrev_b32_e32 v136, 16, v46
	v_and_b32_e32 v143, 0xffff0000, v50
	v_lshlrev_b32_e32 v50, 16, v51
	v_mul_f32_e32 v46, 0x45800000, v83
	v_cndmask_b32_e32 v46, v83, v46, vcc
	v_pk_mul_f32 v[134:135], v[46:47], v[134:135] op_sel_hi:[0,1]
	v_pk_mul_f32 v[114:115], v[46:47], v[114:115] op_sel_hi:[0,1]
	v_pk_mul_f32 v[116:117], v[46:47], v[116:117] op_sel_hi:[0,1]
	v_pk_mul_f32 v[88:89], v[46:47], v[88:89] op_sel_hi:[0,1]
	v_pk_mul_f32 v[130:131], v[180:181], v[134:135]
	v_pk_mul_f32 v[72:73], v[176:177], v[114:115]
	v_pk_mul_f32 v[114:115], v[182:183], v[116:117]
	v_pk_mul_f32 v[74:75], v[178:179], v[88:89]
	v_pk_mul_f32 v[88:89], v[130:131], v[140:141]
	v_pk_mul_f32 v[112:113], v[72:73], v[112:113]
	v_pk_mul_f32 v[114:115], v[114:115], v[138:139]
	v_pk_mul_f32 v[86:87], v[74:75], v[86:87]
	v_cvt_pk_bf16_f32 v72, v88, v89
	v_cvt_pk_bf16_f32 v73, v114, v115
	v_cvt_pk_bf16_f32 v74, v112, v113
	v_cvt_pk_bf16_f32 v75, v86, v87
	global_store_dwordx4 v[78:79], v[72:75], off offset:3072
	s_nop 0
	v_lshlrev_b32_e32 v112, 16, v55
	v_and_b32_e32 v113, 0xffff0000, v47
	v_lshlrev_b32_e32 v46, 16, v47
	v_and_b32_e32 v47, 0xffff0000, v55
	v_and_b32_e32 v55, 0xffff0000, v48
	v_lshlrev_b32_e32 v114, 16, v48
	v_and_b32_e32 v115, 0xffff0000, v56
	v_lshlrev_b32_e32 v130, 16, v57
	v_and_b32_e32 v131, 0xffff0000, v49
	v_lshlrev_b32_e32 v48, 16, v49
	v_and_b32_e32 v49, 0xffff0000, v57
	v_sub_f32_e32 v56, v126, v129
	v_sub_f32_e32 v57, v127, v129
	v_sub_f32_e32 v83, v128, v129
	v_mul_f32_e32 v56, 0x3fb8aa3b, v56
	v_mul_f32_e32 v126, 0x3fb8aa3b, v57
	v_mul_f32_e32 v83, 0x3fb8aa3b, v83
	v_exp_f32_e32 v57, v56
	v_exp_f32_e32 v56, v126
	v_exp_f32_e32 v83, v83
	v_add_co_u32_e32 v80, vcc, s31, v80
	v_add_f32_e32 v126, v57, v56
	v_add_f32_e32 v126, v83, v126
	v_div_scale_f32 v127, s[34:35], v126, v126, 1.0
	v_rcp_f32_e32 v128, v127
	v_addc_co_u32_e32 v81, vcc, 0, v81, vcc
	v_div_scale_f32 v129, vcc, 1.0, v126, 1.0
	v_fma_f32 v132, -v127, v128, 1.0
	v_fmac_f32_e32 v128, v132, v128
	v_mul_f32_e32 v132, v129, v128
	v_fma_f32 v133, -v127, v132, v129
	v_fmac_f32_e32 v132, v133, v128
	v_fma_f32 v127, -v127, v132, v129
	v_div_fmas_f32 v127, v127, v128, v132
	v_div_fixup_f32 v126, v127, v126, 1.0
	v_pk_mul_f32 v[56:57], v[56:57], v[126:127] op_sel_hi:[1,0]
	v_and_b32_e32 v51, 0xffff0000, v51
	v_pk_mul_f32 v[46:47], v[56:57], v[46:47] op_sel:[1,0] op_sel_hi:[0,1]
	v_mul_f32_e32 v128, v83, v126
	v_pk_mul_f32 v[126:127], v[56:57], v[136:137] op_sel:[1,0] op_sel_hi:[0,1]
	v_pk_fma_f32 v[46:47], v[56:57], v[112:113], v[46:47]
	s_andn2_b64 vcc, exec, s[4:5]
	v_pk_mul_f32 v[114:115], v[56:57], v[114:115] op_sel:[1,0] op_sel_hi:[0,1]
	v_pk_mul_f32 v[48:49], v[56:57], v[48:49] op_sel:[1,0] op_sel_hi:[0,1]
	v_pk_fma_f32 v[58:59], v[56:57], v[58:59], v[126:127]
	v_pk_fma_f32 v[50:51], v[128:129], v[50:51], v[46:47] op_sel_hi:[0,1,1]
	v_mul_f32_e32 v47, 0x4b800000, v82
	v_cmp_gt_f32_e64 s[4:5], s29, v82
	v_pk_fma_f32 v[54:55], v[56:57], v[54:55], v[114:115]
	v_pk_fma_f32 v[48:49], v[56:57], v[130:131], v[48:49]
	v_pk_fma_f32 v[56:57], v[128:129], v[142:143], v[58:59] op_sel_hi:[0,1,1]
	v_cndmask_b32_e64 v47, v82, v47, s[4:5]
	v_cvt_pk_bf16_f32 v46, v56, v57
	v_rsq_f32_e32 v56, v47
	v_lshlrev_b32_e32 v116, 16, v52
	v_and_b32_e32 v117, 0xffff0000, v52
	v_lshlrev_b32_e32 v52, 16, v53
	v_and_b32_e32 v53, 0xffff0000, v53
	v_cvt_pk_bf16_f32 v47, v50, v51
	v_mul_f32_e32 v50, 0x45800000, v56
	v_pk_fma_f32 v[54:55], v[128:129], v[116:117], v[54:55] op_sel_hi:[0,1,1]
	v_pk_fma_f32 v[52:53], v[128:129], v[52:53], v[48:49] op_sel_hi:[0,1,1]
	v_cndmask_b32_e64 v50, v56, v50, s[4:5]
	v_cvt_pk_bf16_f32 v48, v54, v55
	v_cvt_pk_bf16_f32 v49, v52, v53
	v_pk_mul_f32 v[52:53], v[50:51], v[84:85] op_sel_hi:[0,1]
	v_pk_mul_f32 v[54:55], v[50:51], v[76:77] op_sel_hi:[0,1]
	v_pk_mul_f32 v[56:57], v[50:51], v[68:69] op_sel_hi:[0,1]
	v_pk_mul_f32 v[50:51], v[50:51], v[70:71] op_sel_hi:[0,1]
	v_pk_mul_f32 v[54:55], v[184:185], v[54:55]
	v_pk_mul_f32 v[52:53], v[188:189], v[52:53]
	v_pk_mul_f32 v[56:57], v[190:191], v[56:57]
	v_pk_mul_f32 v[50:51], v[186:187], v[50:51]
	v_pk_mul_f32 v[52:53], v[52:53], v[66:67]
	v_pk_mul_f32 v[54:55], v[54:55], v[64:65]
	v_pk_mul_f32 v[56:57], v[56:57], v[60:61]
	v_pk_mul_f32 v[58:59], v[50:51], v[62:63]
	v_cvt_pk_bf16_f32 v50, v52, v53
	v_cvt_pk_bf16_f32 v51, v56, v57
	v_cvt_pk_bf16_f32 v52, v54, v55
	v_cvt_pk_bf16_f32 v53, v58, v59
	global_store_dwordx4 v[80:81], v[50:53], off
	global_store_dwordx4 v[78:79], v[46:49], off
	s_cbranch_vccnz .LBB0_527
; DI unsigned pk2(float lo, float hi) { return cvtpk_s(lo, hi); }
; DI void p4_store(const P4Row& R, const float* hg, bf16_t* YC, int row, int lane) {
; #pragma unroll
;     for (int j = 0; j < 4; ++j) {
;         const int c0 = 512 * j + 8 * lane; const u32x4 o = R.o[j], sg = R.sg[j];
;         float v[8] = {bflo(o.x), bfhi(o.x), bflo(o.y), bfhi(o.y), bflo(o.z), bfhi(o.z), bflo(o.w), bfhi(o.w)};
;         const float s[8] = {bflo(sg.x), bfhi(sg.x), bflo(sg.y), bfhi(sg.y), bflo(sg.z), bfhi(sg.z), bflo(sg.w), bfhi(sg.w)};
;         float ss = 0.f;
; #pragma unroll
;         for (int e = 0; e < 8; ++e) ss += v[e] * v[e];
;         ss += __shfl_xor(ss, 1); ss += __shfl_xor(ss, 2); ss += __shfl_xor(ss, 4); ss += __shfl_xor(ss, 8);
;         const float rinv = rsqrtf(ss * (1.0f / 128.0f) + EPS);
;         const f32x4 g0 = *(const f32x4*)(hg + c0), g1 = *(const f32x4*)(hg + c0 + 4);
; #pragma unroll
;         for (int e = 0; e < 4; ++e) { v[e] = v[e] * rinv * g0[e] * s[e]; v[4 + e] = v[4 + e] * rinv * g1[e] * s[4 + e]; }
;         u32x4 w; w.x = pk2(v[0], v[1]); w.y = pk2(v[2], v[3]); w.z = pk2(v[4], v[5]); w.w = pk2(v[6], v[7]);
;         *(u32x4*)(YC + (size_t)row * KCAT + 512 + c0) = w;
;     }
	v_and_b32_e32 v67, 0xffff0000, v2
	v_and_b32_e32 v81, 0xffff0000, v6
	v_lshlrev_b32_e32 v62, 16, v3
	v_and_b32_e32 v63, 0xffff0000, v3
	v_lshlrev_b32_e32 v66, 16, v2
	v_lshlrev_b32_e32 v76, 16, v7
	v_and_b32_e32 v77, 0xffff0000, v7
	v_lshlrev_b32_e32 v80, 16, v6
	v_mov_b32_e32 v84, v81
	v_mov_b32_e32 v85, v67
	v_pk_mul_f32 v[64:65], v[62:63], v[62:63]
	v_pk_mul_f32 v[78:79], v[76:77], v[76:77]
	v_mov_b32_e32 v82, v80
	v_mov_b32_e32 v83, v66
	v_pk_mul_f32 v[84:85], v[84:85], v[84:85]
	v_lshlrev_b32_e32 v58, 16, v4
	v_and_b32_e32 v59, 0xffff0000, v4
	v_lshlrev_b32_e32 v72, 16, v8
	v_and_b32_e32 v73, 0xffff0000, v8
	v_pk_fma_f32 v[82:83], v[82:83], v[82:83], v[84:85]
	v_mov_b32_e32 v84, v78
	v_mov_b32_e32 v85, v64
	v_pk_mul_f32 v[60:61], v[58:59], v[58:59]
	v_pk_mul_f32 v[74:75], v[72:73], v[72:73]
	v_pk_add_f32 v[82:83], v[84:85], v[82:83]
	v_mov_b32_e32 v64, v79
	v_lshlrev_b32_e32 v54, 16, v5
	v_and_b32_e32 v55, 0xffff0000, v5
	v_lshlrev_b32_e32 v68, 16, v9
	v_and_b32_e32 v69, 0xffff0000, v9
	v_pk_add_f32 v[64:65], v[64:65], v[82:83]
	v_mov_b32_e32 v78, v74
	v_mov_b32_e32 v79, v60
	v_pk_mul_f32 v[56:57], v[54:55], v[54:55]
	v_pk_mul_f32 v[70:71], v[68:69], v[68:69]
	v_pk_add_f32 v[64:65], v[78:79], v[64:65]
	v_mov_b32_e32 v60, v75
	v_pk_add_f32 v[60:61], v[60:61], v[64:65]
	v_mov_b32_e32 v64, v70
	v_mov_b32_e32 v65, v56
	v_pk_add_f32 v[60:61], v[64:65], v[60:61]
	v_mov_b32_e32 v56, v71
	v_pk_add_f32 v[56:57], v[56:57], v[60:61]
	ds_bpermute_b32 v61, v1, v57
	ds_bpermute_b32 v60, v1, v56
	v_mov_b64_e32 v[82:83], s[22:23]
	v_lshlrev_b32_e32 v70, 16, v16
	v_and_b32_e32 v71, 0xffff0000, v16
	v_lshlrev_b32_e32 v74, 16, v15
	s_waitcnt lgkmcnt(0)
	v_pk_add_f32 v[56:57], v[56:57], v[60:61]
	ds_bpermute_b32 v61, v118, v57
	ds_bpermute_b32 v60, v118, v56
	v_and_b32_e32 v75, 0xffff0000, v15
	s_mul_i32 s4, s24, 0x1400
	v_lshlrev_b32_e32 v64, 16, v17
	v_and_b32_e32 v65, 0xffff0000, v17
	s_waitcnt lgkmcnt(0)
	v_pk_add_f32 v[56:57], v[56:57], v[60:61]
	ds_bpermute_b32 v61, v119, v57
	ds_bpermute_b32 v60, v119, v56
	v_lshlrev_b32_e32 v78, 16, v14
	v_and_b32_e32 v79, 0xffff0000, v14
	s_mul_hi_i32 s5, s24, 0x1400
	s_add_u32 s4, s3, s4
	s_waitcnt lgkmcnt(0)
	v_pk_add_f32 v[56:57], v[56:57], v[60:61]
	ds_bpermute_b32 v61, v120, v57
	ds_bpermute_b32 v60, v120, v56
	s_addc_u32 s5, s21, s5
	v_lshlrev_b32_e32 v114, 16, v37
	v_lshlrev_b32_e32 v112, 16, v41
	v_and_b32_e32 v113, 0xffff0000, v37
	s_waitcnt lgkmcnt(0)
	v_pk_add_f32 v[56:57], v[56:57], v[60:61]
	v_lshlrev_b32_e32 v126, 16, v45
	v_pk_fma_f32 v[56:57], v[56:57], s[20:21], v[82:83] op_sel_hi:[1,0,0]
	s_nop 0
	v_mul_f32_e32 v60, 0x4b800000, v57
	v_cmp_gt_f32_e32 vcc, s29, v57
	s_nop 1
	v_cndmask_b32_e32 v57, v57, v60, vcc
	v_rsq_f32_e32 v57, v57
	s_nop 0
	v_mul_f32_e32 v60, 0x45800000, v57
	v_cndmask_b32_e32 v60, v57, v60, vcc
	v_pk_mul_f32 v[58:59], v[60:61], v[58:59] op_sel_hi:[0,1]
	v_pk_mul_f32 v[46:47], v[160:161], v[58:59]
	v_pk_mul_f32 v[66:67], v[60:61], v[66:67] op_sel_hi:[0,1]
	v_pk_mul_f32 v[58:59], v[46:47], v[70:71]
	v_pk_mul_f32 v[46:47], v[60:61], v[62:63] op_sel_hi:[0,1]
	v_pk_mul_f32 v[46:47], v[166:167], v[46:47]
	v_pk_mul_f32 v[50:51], v[164:165], v[66:67]
	v_pk_mul_f32 v[52:53], v[46:47], v[74:75]
	v_pk_mul_f32 v[46:47], v[60:61], v[54:55] op_sel_hi:[0,1]
	v_pk_mul_f32 v[46:47], v[162:163], v[46:47]
	v_pk_mul_f32 v[50:51], v[50:51], v[78:79]
	v_pk_mul_f32 v[54:55], v[46:47], v[64:65]
	v_cvt_pk_bf16_f32 v46, v50, v51
	v_cvt_pk_bf16_f32 v47, v52, v53
	v_cvt_pk_bf16_f32 v48, v58, v59
	v_cvt_pk_bf16_f32 v49, v54, v55
	global_store_dwordx4 v121, v[46:49], s[4:5] offset:1024
	s_nop 0
	v_mul_f32_e32 v57, 0x4b800000, v56
	v_cmp_gt_f32_e32 vcc, s29, v56
	v_lshlrev_b32_e32 v54, 16, v21
	v_and_b32_e32 v55, 0xffff0000, v21
	v_cndmask_b32_e32 v56, v56, v57, vcc
	v_rsq_f32_e32 v56, v56
	v_lshlrev_b32_e32 v58, 16, v20
	v_and_b32_e32 v59, 0xffff0000, v20
	v_lshlrev_b32_e32 v60, 16, v19
	v_mul_f32_e32 v57, 0x45800000, v56
	v_cndmask_b32_e32 v56, v56, v57, vcc
	v_pk_mul_f32 v[74:75], v[56:57], v[80:81] op_sel_hi:[0,1]
	v_pk_mul_f32 v[72:73], v[56:57], v[72:73] op_sel_hi:[0,1]
	v_pk_mul_f32 v[76:77], v[56:57], v[76:77] op_sel_hi:[0,1]
	v_pk_mul_f32 v[56:57], v[56:57], v[68:69] op_sel_hi:[0,1]
	v_and_b32_e32 v61, 0xffff0000, v19
	v_lshlrev_b32_e32 v62, 16, v18
	v_and_b32_e32 v63, 0xffff0000, v18
	v_lshlrev_b32_e32 v64, 16, v13
	v_and_b32_e32 v65, 0xffff0000, v13
	v_lshlrev_b32_e32 v66, 16, v12
	v_and_b32_e32 v67, 0xffff0000, v12
	v_lshlrev_b32_e32 v70, 16, v11
	v_and_b32_e32 v71, 0xffff0000, v11
	v_pk_mul_f32 v[68:69], v[64:65], v[64:65]
	v_pk_mul_f32 v[46:47], v[168:169], v[74:75]
	v_pk_mul_f32 v[50:51], v[172:173], v[72:73]
	v_pk_mul_f32 v[48:49], v[170:171], v[76:77]
	v_pk_mul_f32 v[52:53], v[174:175], v[56:57]
	v_pk_mul_f32 v[46:47], v[46:47], v[62:63]
	v_pk_mul_f32 v[50:51], v[50:51], v[58:59]
	v_pk_mul_f32 v[48:49], v[48:49], v[60:61]
	v_pk_mul_f32 v[52:53], v[52:53], v[54:55]
	v_cvt_pk_bf16_f32 v46, v46, v47
	v_cvt_pk_bf16_f32 v47, v48, v49
	v_cvt_pk_bf16_f32 v48, v50, v51
	v_cvt_pk_bf16_f32 v49, v52, v53
	global_store_dwordx4 v121, v[46:49], s[4:5] offset:2048
	v_and_b32_e32 v63, 0xffff0000, v10
	v_and_b32_e32 v53, 0xffff0000, v22
	v_lshlrev_b32_e32 v62, 16, v10
	v_lshlrev_b32_e32 v46, 16, v25
	v_and_b32_e32 v47, 0xffff0000, v25
	v_lshlrev_b32_e32 v48, 16, v24
	v_and_b32_e32 v49, 0xffff0000, v24
	v_lshlrev_b32_e32 v50, 16, v23
	v_and_b32_e32 v51, 0xffff0000, v23
	v_lshlrev_b32_e32 v52, 16, v22
	v_mov_b32_e32 v86, v53
	v_mov_b32_e32 v87, v63
	v_pk_mul_f32 v[72:73], v[66:67], v[66:67]
	v_pk_mul_f32 v[74:75], v[70:71], v[70:71]
	v_pk_mul_f32 v[76:77], v[46:47], v[46:47]
	v_pk_mul_f32 v[78:79], v[48:49], v[48:49]
	v_pk_mul_f32 v[80:81], v[50:51], v[50:51]
	v_mov_b32_e32 v84, v52
	v_mov_b32_e32 v85, v62
	v_pk_mul_f32 v[86:87], v[86:87], v[86:87]
	v_mov_b32_e32 v88, v80
	v_mov_b32_e32 v89, v74
	v_mov_b32_e32 v74, v81
	v_mov_b32_e32 v80, v78
	v_mov_b32_e32 v81, v72
	v_mov_b32_e32 v72, v79
	v_mov_b32_e32 v78, v76
	v_mov_b32_e32 v79, v68
	v_mov_b32_e32 v68, v77
	v_pk_fma_f32 v[76:77], v[84:85], v[84:85], v[86:87]
	v_lshlrev_b32_e32 v84, 16, v33
	v_pk_add_f32 v[76:77], v[88:89], v[76:77]
	v_and_b32_e32 v85, 0xffff0000, v33
	v_pk_add_f32 v[74:75], v[74:75], v[76:77]
	v_lshlrev_b32_e32 v76, 16, v28
	v_pk_add_f32 v[74:75], v[80:81], v[74:75]
	v_and_b32_e32 v77, 0xffff0000, v28
	v_pk_add_f32 v[72:73], v[72:73], v[74:75]
	v_lshlrev_b32_e32 v74, 16, v29
	v_pk_add_f32 v[72:73], v[78:79], v[72:73]
	v_and_b32_e32 v75, 0xffff0000, v29
	v_pk_add_f32 v[68:69], v[68:69], v[72:73]
	ds_bpermute_b32 v73, v1, v69
	ds_bpermute_b32 v72, v1, v68
	v_lshlrev_b32_e32 v78, 16, v27
	v_and_b32_e32 v79, 0xffff0000, v27
	v_lshlrev_b32_e32 v80, 16, v26
	v_and_b32_e32 v81, 0xffff0000, v26
	s_waitcnt lgkmcnt(0)
; DI unsigned pk2(float lo, float hi) { return cvtpk_s(lo, hi); }
; DI void p4_store(const P4Row& R, const float* hg, bf16_t* YC, int row, int lane) {
; #pragma unroll
;     for (int j = 0; j < 4; ++j) {
;         const int c0 = 512 * j + 8 * lane; const u32x4 o = R.o[j], sg = R.sg[j];
;         float v[8] = {bflo(o.x), bfhi(o.x), bflo(o.y), bfhi(o.y), bflo(o.z), bfhi(o.z), bflo(o.w), bfhi(o.w)};
;         const float s[8] = {bflo(sg.x), bfhi(sg.x), bflo(sg.y), bfhi(sg.y), bflo(sg.z), bfhi(sg.z), bflo(sg.w), bfhi(sg.w)};
;         float ss = 0.f;
; #pragma unroll
;         for (int e = 0; e < 8; ++e) ss += v[e] * v[e];
;         ss += __shfl_xor(ss, 1); ss += __shfl_xor(ss, 2); ss += __shfl_xor(ss, 4); ss += __shfl_xor(ss, 8);
;         const float rinv = rsqrtf(ss * (1.0f / 128.0f) + EPS);
;         const f32x4 g0 = *(const f32x4*)(hg + c0), g1 = *(const f32x4*)(hg + c0 + 4);
; #pragma unroll
;         for (int e = 0; e < 4; ++e) { v[e] = v[e] * rinv * g0[e] * s[e]; v[4 + e] = v[4 + e] * rinv * g1[e] * s[4 + e]; }
;         u32x4 w; w.x = pk2(v[0], v[1]); w.y = pk2(v[2], v[3]); w.z = pk2(v[4], v[5]); w.w = pk2(v[6], v[7]);
;         *(u32x4*)(YC + (size_t)row * KCAT + 512 + c0) = w;
;     }
;     {
;         const int c0 = 8 * lane; const float l0 = R.l0, l1 = R.l1, l2 = R.l2; const u32x4 x0 = R.x0, x1 = R.x1, x2 = R.x2;
;         const float mx = fmaxf(l0, fmaxf(l1, l2)); float a0 = __expf(l0 - mx), a1 = __expf(l1 - mx), a2 = __expf(l2 - mx);
;         const float inv = 1.0f / (a0 + a1 + a2); a0 *= inv; a1 *= inv; a2 *= inv;
;         u32x4 w;
;         w.x = pk2(a0 * bflo(x0.x) + a1 * bflo(x1.x) + a2 * bflo(x2.x), a0 * bfhi(x0.x) + a1 * bfhi(x1.x) + a2 * bfhi(x2.x));
;         w.y = pk2(a0 * bflo(x0.y) + a1 * bflo(x1.y) + a2 * bflo(x2.y), a0 * bfhi(x0.y) + a1 * bfhi(x1.y) + a2 * bfhi(x2.y));
;         w.z = pk2(a0 * bflo(x0.z) + a1 * bflo(x1.z) + a2 * bflo(x2.z), a0 * bfhi(x0.z) + a1 * bfhi(x1.z) + a2 * bfhi(x2.z));
;         w.w = pk2(a0 * bflo(x0.w) + a1 * bflo(x1.w) + a2 * bflo(x2.w), a0 * bfhi(x0.w) + a1 * bfhi(x1.w) + a2 * bfhi(x2.w));
;         *(u32x4*)(YC + (size_t)row * KCAT + c0) = w;
;     }
; }
	v_pk_add_f32 v[68:69], v[68:69], v[72:73]
	ds_bpermute_b32 v73, v118, v69
	ds_bpermute_b32 v72, v118, v68
	v_lshlrev_b32_e32 v86, 16, v32
	v_and_b32_e32 v87, 0xffff0000, v32
	s_waitcnt lgkmcnt(0)
	v_pk_add_f32 v[68:69], v[68:69], v[72:73]
	ds_bpermute_b32 v73, v119, v69
	ds_bpermute_b32 v72, v119, v68
	s_waitcnt lgkmcnt(0)
	v_pk_add_f32 v[68:69], v[68:69], v[72:73]
	ds_bpermute_b32 v73, v120, v69
	ds_bpermute_b32 v72, v120, v68
	s_waitcnt lgkmcnt(0)
	v_pk_add_f32 v[68:69], v[68:69], v[72:73]
	s_nop 0
	v_pk_fma_f32 v[68:69], v[68:69], s[20:21], v[82:83] op_sel_hi:[1,0,0]
	v_and_b32_e32 v73, 0xffff0000, v31
	v_mul_f32_e32 v72, 0x4b800000, v69
	v_cmp_gt_f32_e32 vcc, s29, v69
	v_lshlrev_b32_e32 v82, 16, v30
	s_nop 0
	v_cndmask_b32_e32 v69, v69, v72, vcc
	v_rsq_f32_e32 v69, v69
	v_lshlrev_b32_e32 v72, 16, v31
	v_mul_f32_e32 v83, 0x45800000, v69
	v_cndmask_b32_e32 v88, v69, v83, vcc
	v_pk_mul_f32 v[62:63], v[88:89], v[62:63] op_sel_hi:[0,1]
	v_pk_mul_f32 v[66:67], v[88:89], v[66:67] op_sel_hi:[0,1]
	v_pk_mul_f32 v[70:71], v[88:89], v[70:71] op_sel_hi:[0,1]
	v_pk_mul_f32 v[64:65], v[88:89], v[64:65] op_sel_hi:[0,1]
	v_pk_mul_f32 v[58:59], v[180:181], v[62:63]
	v_pk_mul_f32 v[54:55], v[176:177], v[66:67]
	v_pk_mul_f32 v[60:61], v[182:183], v[70:71]
	v_pk_mul_f32 v[56:57], v[178:179], v[64:65]
	v_pk_mul_f32 v[58:59], v[58:59], v[80:81]
	v_pk_mul_f32 v[62:63], v[54:55], v[76:77]
	v_pk_mul_f32 v[60:61], v[60:61], v[78:79]
	v_pk_mul_f32 v[64:65], v[56:57], v[74:75]
	v_cvt_pk_bf16_f32 v54, v58, v59
	v_cvt_pk_bf16_f32 v55, v60, v61
	v_cvt_pk_bf16_f32 v56, v62, v63
	v_cvt_pk_bf16_f32 v57, v64, v65
	global_store_dwordx4 v121, v[54:57], s[4:5] offset:3072
	s_nop 0
	v_max3_f32 v69, v123, v124, v125
	v_sub_f32_e32 v115, v123, v69
	v_sub_f32_e32 v116, v124, v69
	v_sub_f32_e32 v69, v125, v69
	v_mul_f32_e32 v115, 0x3fb8aa3b, v115
	v_mul_f32_e32 v116, 0x3fb8aa3b, v116
	v_mul_f32_e32 v69, 0x3fb8aa3b, v69
	v_exp_f32_e32 v117, v115
	v_exp_f32_e32 v116, v116
	v_exp_f32_e32 v69, v69
	v_lshlrev_b32_e32 v64, 16, v34
	v_and_b32_e32 v65, 0xffff0000, v38
	v_add_f32_e32 v127, v117, v116
	v_add_f32_e32 v128, v69, v127
	v_div_scale_f32 v129, s[24:25], v128, v128, 1.0
	v_rcp_f32_e32 v130, v129
	v_div_scale_f32 v131, vcc, 1.0, v128, 1.0
	v_lshlrev_b32_e32 v62, 16, v38
	v_fma_f32 v132, -v129, v130, 1.0
	v_fmac_f32_e32 v130, v132, v130
	v_mul_f32_e32 v132, v131, v130
	v_fma_f32 v133, -v129, v132, v131
	v_fmac_f32_e32 v132, v133, v130
	v_fma_f32 v129, -v129, v132, v131
	v_div_fmas_f32 v129, v129, v130, v132
	v_div_fixup_f32 v128, v129, v128, 1.0
	v_pk_mul_f32 v[116:117], v[116:117], v[128:129] op_sel_hi:[1,0]
	v_and_b32_e32 v63, 0xffff0000, v34
	v_pk_mul_f32 v[64:65], v[116:117], v[64:65] op_sel:[1,0] op_sel_hi:[0,1]
	v_lshlrev_b32_e32 v66, 16, v42
	v_and_b32_e32 v67, 0xffff0000, v42
	v_mul_f32_e32 v130, v69, v128
	v_pk_fma_f32 v[62:63], v[116:117], v[62:63], v[64:65]
	v_cmp_gt_f32_e32 vcc, s29, v68
	v_pk_fma_f32 v[62:63], v[130:131], v[66:67], v[62:63] op_sel_hi:[0,1,1]
	v_cvt_pk_bf16_f32 v62, v62, v63
	v_mul_f32_e32 v63, 0x4b800000, v68
	v_cndmask_b32_e32 v63, v68, v63, vcc
	v_lshlrev_b32_e32 v74, 16, v35
	v_and_b32_e32 v75, 0xffff0000, v39
	v_lshlrev_b32_e32 v80, 16, v36
	v_and_b32_e32 v81, 0xffff0000, v40
	v_rsq_f32_e32 v68, v63
	v_lshlrev_b32_e32 v70, 16, v39
	v_and_b32_e32 v71, 0xffff0000, v35
	v_lshlrev_b32_e32 v78, 16, v40
	v_and_b32_e32 v79, 0xffff0000, v36
	v_pk_mul_f32 v[74:75], v[116:117], v[74:75] op_sel:[1,0] op_sel_hi:[0,1]
	v_pk_mul_f32 v[80:81], v[116:117], v[80:81] op_sel:[1,0] op_sel_hi:[0,1]
	v_lshlrev_b32_e32 v76, 16, v43
	v_and_b32_e32 v77, 0xffff0000, v43
	v_lshlrev_b32_e32 v88, 16, v44
	v_and_b32_e32 v89, 0xffff0000, v44
	v_pk_fma_f32 v[64:65], v[116:117], v[70:71], v[74:75]
	v_pk_fma_f32 v[70:71], v[116:117], v[78:79], v[80:81]
	v_pk_fma_f32 v[64:65], v[130:131], v[76:77], v[64:65] op_sel_hi:[0,1,1]
	v_pk_fma_f32 v[66:67], v[130:131], v[88:89], v[70:71] op_sel_hi:[0,1,1]
	v_cvt_pk_bf16_f32 v63, v64, v65
	v_cvt_pk_bf16_f32 v64, v66, v67
	v_mul_f32_e32 v66, 0x45800000, v68
	v_cndmask_b32_e32 v66, v68, v66, vcc
	v_and_b32_e32 v115, 0xffff0000, v41
	v_pk_mul_f32 v[52:53], v[66:67], v[52:53] op_sel_hi:[0,1]
	v_pk_mul_f32 v[48:49], v[66:67], v[48:49] op_sel_hi:[0,1]
	v_pk_mul_f32 v[50:51], v[66:67], v[50:51] op_sel_hi:[0,1]
	v_pk_mul_f32 v[46:47], v[66:67], v[46:47] op_sel_hi:[0,1]
	v_and_b32_e32 v83, 0xffff0000, v30
	v_pk_mul_f32 v[114:115], v[116:117], v[114:115] op_sel:[1,0] op_sel_hi:[0,1]
	v_and_b32_e32 v127, 0xffff0000, v45
	v_pk_fma_f32 v[74:75], v[116:117], v[112:113], v[114:115]
	v_pk_mul_f32 v[48:49], v[184:185], v[48:49]
	v_pk_mul_f32 v[52:53], v[188:189], v[52:53]
	v_pk_mul_f32 v[50:51], v[190:191], v[50:51]
	v_pk_mul_f32 v[46:47], v[186:187], v[46:47]
	v_pk_mul_f32 v[52:53], v[52:53], v[82:83]
	v_pk_mul_f32 v[48:49], v[48:49], v[86:87]
	v_pk_mul_f32 v[50:51], v[50:51], v[72:73]
	v_pk_mul_f32 v[54:55], v[46:47], v[84:85]
	v_pk_fma_f32 v[70:71], v[130:131], v[126:127], v[74:75] op_sel_hi:[0,1,1]
	v_cvt_pk_bf16_f32 v46, v52, v53
	v_cvt_pk_bf16_f32 v47, v50, v51
	v_cvt_pk_bf16_f32 v48, v48, v49
	v_cvt_pk_bf16_f32 v49, v54, v55
	v_cvt_pk_bf16_f32 v65, v70, v71
	global_store_dwordx4 v122, v[46:49], s[4:5] offset:1024
	global_store_dwordx4 v121, v[62:65], s[4:5]
	s_branch .LBB0_527
